# speedup vs baseline: 1.0327x; 1.0100x over previous
_Z8moe_gemmILi1024ELi2048ELb1EEvPKDF16_S1_PKfPDF16_PfPKiS7_:
	v_lshl_or_b32 v216, s2, 8, v0
	v_and_b32_e32 v217, 63, v216
	v_lshrrev_b32_e32 v216, 6, v216
	v_lshlrev_b32_e32 v215, 3, v217
	v_lshlrev_b32_e32 v214, 4, v217
	v_lshl_add_u32 v217, v216, 10, v215
	v_lshl_add_u32 v216, v216, 11, v214
	s_mov_b32 s96, 16
	s_mov_b32 s97, 0
	s_mov_b32 s98, 0
	s_and_b32 s90, s2, 7
	s_lshr_b32 s91, s2, 3
	v_readfirstlane_b32 s88, v0
	s_load_dwordx2 s[4:5], s[0:1], 0x28
	v_readfirstlane_b32 s12, v0
	s_waitcnt lgkmcnt(0)
	s_load_dwordx2 s[92:93], s[4:5], 0x400
	s_add_u32 s94, s4, 0x6000000
	s_addc_u32 s95, s5, 0
	s_load_dword s23, s[4:5], 0x0
	s_load_dword s25, s[4:5], 0x80
	s_load_dword s27, s[4:5], 0x100
	s_load_dword s29, s[4:5], 0x180
	s_load_dword s31, s[4:5], 0x200
	s_load_dword s33, s[4:5], 0x280
	s_load_dword s35, s[4:5], 0x300
	s_load_dword s38, s[4:5], 0x380
	s_waitcnt lgkmcnt(0)
	global_load_dwordx4 v[218:221], v216, s[92:93] nt
	global_load_dwordx4 v[222:225], v216, s[92:93] offset:1024 nt
	s_add_u32 s92, s92, 0x400000
	s_addc_u32 s93, s93, 0
	global_load_dwordx4 v[226:229], v216, s[92:93] nt
	global_load_dwordx4 v[230:233], v216, s[92:93] offset:1024 nt
	s_add_u32 s92, s92, 0x400000
	s_addc_u32 s93, s93, 0
	global_load_dwordx4 v[234:237], v216, s[92:93] nt
	global_load_dwordx4 v[238:241], v216, s[92:93] offset:1024 nt
	s_add_u32 s92, s92, 0x400000
	s_addc_u32 s93, s93, 0
	global_load_dwordx4 v[242:245], v216, s[92:93] nt
	global_load_dwordx4 v[246:249], v216, s[92:93] offset:1024 nt
	s_add_u32 s92, s92, 0x400000
	s_addc_u32 s93, s93, 0
	s_mov_b32 s100, 1
	s_add_i32 s3, s23, 0x9f
	s_mul_hi_i32 s3, s3, 0x66666667
	s_lshr_b32 s4, s3, 31
	s_ashr_i32 s39, s3, 6
	s_add_i32 s3, s25, 0x9f
	s_mul_hi_i32 s3, s3, 0x66666667
	s_add_i32 s39, s39, s4
	s_lshr_b32 s4, s3, 31
	s_ashr_i32 s40, s3, 6
	s_add_i32 s40, s40, s4
	s_add_i32 s4, s27, 0x9f
	s_mul_hi_i32 s4, s4, 0x66666667
	s_lshr_b32 s5, s4, 31
	s_ashr_i32 s41, s4, 6
	s_add_i32 s4, s29, 0x9f
	s_mul_hi_i32 s4, s4, 0x66666667
	s_add_i32 s41, s41, s5
	s_lshr_b32 s5, s4, 31
	s_ashr_i32 s42, s4, 6
	s_add_i32 s4, s31, 0x9f
	s_mul_hi_i32 s4, s4, 0x66666667
	s_add_i32 s42, s42, s5
	s_lshr_b32 s5, s4, 31
	s_ashr_i32 s43, s4, 6
	s_add_i32 s4, s33, 0x9f
	s_mul_hi_i32 s4, s4, 0x66666667
	s_add_i32 s3, s40, s39
	s_add_i32 s43, s43, s5
	s_lshr_b32 s5, s4, 31
	s_ashr_i32 s44, s4, 6
	s_add_i32 s4, s35, 0x9f
	s_add_i32 s3, s41, s3
	s_mul_hi_i32 s4, s4, 0x66666667
	s_add_i32 s3, s42, s3
	s_add_i32 s44, s44, s5
	s_lshr_b32 s5, s4, 31
	s_ashr_i32 s45, s4, 6
	s_add_i32 s4, s38, 0x9f
	s_add_i32 s3, s43, s3
	s_mul_hi_i32 s4, s4, 0x66666667
	s_add_i32 s3, s44, s3
	s_add_i32 s45, s45, s5
	s_lshr_b32 s5, s4, 31
	s_ashr_i32 s46, s4, 6
	s_add_i32 s3, s45, s3
	s_add_i32 s46, s46, s5
	s_add_i32 s3, s46, s3
	s_lshl_b32 s3, s3, 4
	s_and_b32 s4, s2, 7
	s_mul_i32 s4, s3, s4
	s_lshr_b32 s2, s2, 3
	s_ashr_i32 s5, s4, 3
	s_add_i32 s4, s4, s3
	s_ashr_i32 s47, s4, 3
	s_add_i32 s48, s5, s2
	s_sub_i32 s89, s47, s5
	s_sub_i32 s89, s89, 64
	s_max_i32 s89, s89, 0
	s_min_i32 s89, s89, 64
	s_add_i32 s99, s48, 64
	s_cmp_lt_i32 s99, s47
	s_cselect_b32 s98, 1, 0
	s_cmp_eq_u32 s98, 0
	s_cbranch_scc1 .Las_set
	s_cmp_ge_i32 s89, 64
	s_cbranch_scc1 .Las_set
	s_mov_b32 s96, 8
	s_mov_b32 s98, 3
.Las_set:
	s_sub_u32 s96, s96, 4
	s_cmp_ge_i32 s48, s47
	s_cbranch_scc1 .LBB2_78
	s_load_dword s13, s[0:1], 0x38
	s_load_dwordx2 s[2:3], s[0:1], 0x30
	s_load_dwordx8 s[4:11], s[0:1], 0x0
	v_bfe_u32 v1, v0, 4, 2
	v_lshrrev_b32_e32 v2, 5, v0
	s_waitcnt lgkmcnt(0)
	s_lshr_b32 s49, s13, 3
	s_bfe_u32 s1, s12, 0x10006
	v_and_or_b32 v2, v2, 4, v1
	v_lshrrev_b32_e32 v5, 7, v0
	s_cmpk_lt_u32 s12, 0x80
	v_lshlrev_b32_e32 v2, 4, v2
	v_lshlrev_b32_e32 v3, 3, v0
	s_movk_i32 s0, 0x78
	v_bfe_u32 v4, v0, 4, 3
	v_bitop3_b32 v5, v5, v0, 7 bitop3:0x78
	v_lshlrev_b32_e32 v6, 6, v0
	s_cselect_b64 s[12:13], -1, 0
	v_bitop3_b32 v2, v2, v3, s0 bitop3:0x78
	v_xor_b32_e32 v5, v5, v4
	s_lshl_b32 s0, s1, 6
	v_lshlrev_b32_e32 v4, 2, v1
	v_lshlrev_b32_e32 v1, 11, v1
	v_and_b32_e32 v6, 0x300, v6
	v_and_b32_e32 v8, 8, v3
	v_lshrrev_b32_e32 v101, 4, v0
	v_and_b32_e32 v103, 15, v0
	v_lshrrev_b32_e32 v124, 3, v0
	v_lshl_add_u32 v125, v0, 4, 0
	v_or3_b32 v1, v1, v6, v8
	v_bfe_u32 v6, v0, 1, 3
	v_or_b32_e32 v0, s0, v4
	v_and_b32_e32 v7, 0xe0, v3
	v_lshl_add_u32 v100, v0, 1, 0
	s_lshl_b32 s1, s1, 7
	v_and_b32_e32 v0, 16, v3
	v_or_b32_e32 v3, s1, v0
	v_bitop3_b32 v0, s1, v7, v0 bitop3:0x36
	v_or_b32_e32 v127, v0, v1
	v_bitop3_b32 v0, v3, v7, 32 bitop3:0x36
	v_or_b32_e32 v128, v0, v1
	v_bitop3_b32 v0, v3, v7, 64 bitop3:0x36
	s_movk_i32 s1, 0x60
	v_or_b32_e32 v129, v0, v1
	v_bitop3_b32 v0, v3, v7, s1 bitop3:0x36
	s_add_i32 s1, s23, 15
	s_lshr_b32 s1, s1, 4
	v_or_b32_e32 v130, v0, v1
	s_add_i32 s1, s39, s1
	v_cvt_f32_i32_e32 v0, s39
	s_add_i32 s1, s1, -1
	v_cvt_f32_i32_e32 v1, s1
	s_add_i32 s14, s25, 15
	v_rcp_iflag_f32_e32 v144, v0
	s_lshr_b32 s14, s14, 4
	v_add_f32_e32 v0, 0.5, v1
	v_cvt_f32_i32_e32 v1, s40
	s_add_i32 s14, s40, s14
	s_add_i32 s14, s14, -1
	v_mul_f32_e32 v0, v144, v0
	v_cvt_i32_f32_e32 v0, v0
	v_cvt_f32_i32_e32 v7, s14
	v_rcp_iflag_f32_e32 v145, v1
	s_add_i32 s16, s27, 15
	s_lshr_b32 s16, s16, 4
	v_cvt_f32_i32_e32 v1, s41
	s_add_i32 s16, s41, s16
	v_readfirstlane_b32 s1, v0
	v_add_f32_e32 v0, 0.5, v7
	s_add_i32 s16, s16, -1
	s_add_i32 s17, s29, 15
	s_add_i32 s18, s31, 15
	s_add_i32 s19, s33, 15
	s_add_i32 s20, s35, 15
	s_add_i32 s21, s38, 15
	v_mul_f32_e32 v0, v145, v0
	s_lshr_b32 s17, s17, 4
	s_lshr_b32 s18, s18, 4
	s_lshr_b32 s19, s19, 4
	s_lshr_b32 s20, s20, 4
	s_lshr_b32 s21, s21, 4
	v_cvt_i32_f32_e32 v0, v0
	v_cvt_f32_i32_e32 v7, s16
	s_add_i32 s17, s42, s17
	s_add_i32 s18, s43, s18
	s_add_i32 s19, s44, s19
	s_add_i32 s20, s45, s20
	s_add_i32 s21, s46, s21
	v_rcp_iflag_f32_e32 v146, v1
	s_add_i32 s50, 0, 0xe000
	s_lshl_b32 s52, s39, 4
	s_lshl_b32 s53, s40, 4
	s_lshl_b32 s54, s41, 4
	s_add_i32 s17, s17, -1
	s_lshl_b32 s55, s42, 4
	s_add_i32 s18, s18, -1
	s_lshl_b32 s56, s43, 4
	s_add_i32 s19, s19, -1
	s_lshl_b32 s57, s44, 4
	s_add_i32 s20, s20, -1
	s_lshl_b32 s58, s45, 4
	s_add_i32 s21, s21, -1
	s_lshl_b32 s59, s46, 4
	s_cmp_gt_i32 s23, 0
	v_cvt_f32_i32_e32 v1, s42
	s_cselect_b32 s60, s1, 0
	v_readfirstlane_b32 s1, v0
	v_add_f32_e32 v0, 0.5, v7
	v_mul_f32_e32 v0, v146, v0
	v_cvt_i32_f32_e32 v0, v0
	v_cvt_f32_i32_e32 v7, s17
	v_rcp_iflag_f32_e32 v147, v1
	s_cmp_gt_i32 s25, 0
	v_cvt_f32_i32_e32 v1, s43
	s_cselect_b32 s61, s1, 0
	v_readfirstlane_b32 s1, v0
	v_add_f32_e32 v0, 0.5, v7
	v_mul_f32_e32 v0, v147, v0
	v_cvt_i32_f32_e32 v0, v0
	v_cvt_f32_i32_e32 v7, s18
	v_rcp_iflag_f32_e32 v148, v1
	s_cmp_gt_i32 s27, 0
	v_cvt_f32_i32_e32 v1, s44
	s_cselect_b32 s62, s1, 0
	v_readfirstlane_b32 s1, v0
	v_add_f32_e32 v0, 0.5, v7
	v_mul_f32_e32 v0, v148, v0
	v_cvt_i32_f32_e32 v0, v0
	v_cvt_f32_i32_e32 v7, s19
	v_rcp_iflag_f32_e32 v149, v1
	s_cmp_gt_i32 s29, 0
	v_cvt_f32_i32_e32 v1, s45
	s_cselect_b32 s63, s1, 0
	v_readfirstlane_b32 s1, v0
	v_add_f32_e32 v0, 0.5, v7
	v_mul_f32_e32 v0, v149, v0
	v_cvt_i32_f32_e32 v0, v0
	v_cvt_f32_i32_e32 v7, s20
	v_rcp_iflag_f32_e32 v150, v1
	s_cmp_gt_i32 s31, 0
	s_cselect_b32 s64, s1, 0
	v_readfirstlane_b32 s1, v0
	v_add_f32_e32 v0, 0.5, v7
	v_mul_f32_e32 v0, v150, v0
	v_cvt_i32_f32_e32 v0, v0
	v_cvt_f32_i32_e32 v1, s46
	s_cmp_gt_i32 s33, 0
	s_cselect_b32 s65, s1, 0
	v_readfirstlane_b32 s1, v0
	v_cvt_f32_i32_e32 v0, s21
	v_rcp_iflag_f32_e32 v151, v1
	v_mov_b32_e32 v97, 0
	v_lshlrev_b32_e32 v96, 12, v101
	v_add_f32_e32 v0, 0.5, v0
	v_mul_f32_e32 v0, v151, v0
	v_cvt_i32_f32_e32 v7, v0
	v_lshlrev_b32_e32 v0, 4, v5
	v_mov_b32_e32 v1, v97
	v_lshl_add_u64 v[98:99], s[6:7], 0, v[96:97]
	s_cmp_gt_i32 s35, 0
	v_lshl_add_u64 v[104:105], s[4:5], 0, v[0:1]
	s_mov_b64 s[4:5], 0x80
	v_lshl_or_b32 v96, v2, 1, v96
	v_lshl_add_u32 v8, v103, 4, 0
	v_mul_u32_u24_e32 v3, 0x110, v101
	s_cselect_b32 s66, s1, 0
	s_cmp_gt_i32 s38, 0
	v_readfirstlane_b32 s1, v7
	v_lshl_add_u64 v[106:107], v[104:105], 0, s[4:5]
	v_lshl_add_u64 v[0:1], s[6:7], 0, v[96:97]
	s_mov_b64 s[4:5], 0x40000
	s_mov_b32 s15, 0
	v_lshlrev_b32_e32 v126, 7, v103
	v_lshlrev_b32_e32 v102, 3, v103
	v_add_u32_e32 v131, s50, v127
	v_add_u32_e32 v132, s50, v128
	v_add_u32_e32 v133, s50, v129
	v_add_u32_e32 v134, s50, v130
	s_movk_i32 s51, 0x110
	v_or_b32_e32 v135, 16, v101
	v_or_b32_e32 v136, 32, v101
	v_or_b32_e32 v137, 48, v101
	v_or_b32_e32 v138, 64, v101
	v_or_b32_e32 v139, 0x50, v101
	v_or_b32_e32 v140, 0x60, v101
	v_or_b32_e32 v141, 0x70, v101
	v_or_b32_e32 v142, 0x80, v101
	v_or_b32_e32 v143, 0x90, v101
	v_bitop3_b32 v152, v6, v101, 3 bitop3:0x78
	s_mul_i32 s67, s52, s60
	s_mul_i32 s68, s53, s61
	s_mul_i32 s69, s54, s62
	s_mul_i32 s70, s55, s63
	s_mul_i32 s71, s56, s64
	s_mul_i32 s72, s57, s65
	s_mul_i32 s73, s58, s66
	s_cselect_b32 s74, s1, 0
	v_lshl_add_u64 v[108:109], v[0:1], 0, s[4:5]
	s_lshl_b32 s6, s0, 2
	v_lshlrev_b32_e32 v153, 2, v4
	v_lshlrev_b32_e32 v96, 1, v2
	s_mov_b64 s[16:17], 0x10000
	s_mov_b64 s[18:19], 0x20000
	s_mov_b64 s[20:21], 0x30000
	s_mov_b32 s22, 0x3f3504f3
	s_mov_b32 s75, 0x3ea7ba05
	s_mov_b32 s24, 0xbfba00e3
	s_mov_b32 s26, 0x3f87dc22
	s_mov_b32 s28, 0x3fb5f0e3
	s_brev_b32 s76, -2
	v_add_u32_e32 v154, v8, v3
	s_movk_i32 s77, 0x1080
	s_mov_b32 s30, 0xbe91a98e
	s_mov_b32 s34, 0x3e827906
	s_branch .LBB2_3

.LBB2_39:
	s_lshl_b32 s36, s79, 4
	v_mul_lo_u32 v155, s36, v1
	v_add_u32_e32 v120, v155, v124
	v_cmp_gt_i32_e32 vcc, s80, v120
	s_lshl_b32 s81, s37, 13
	s_nop 0
	v_cndmask_b32_e32 v1, 0, v120, vcc
	v_add_u32_e32 v2, s81, v1
	v_add_u32_e32 v1, 32, v120
	v_cmp_gt_i32_e32 vcc, s80, v1
	v_ashrrev_i32_e32 v3, 31, v2
	v_lshl_add_u64 v[2:3], v[2:3], 2, s[2:3]
	v_cndmask_b32_e32 v1, 0, v1, vcc
	v_add_u32_e32 v4, s81, v1
	v_add_u32_e32 v1, 64, v120
	v_cmp_gt_i32_e32 vcc, s80, v1
	v_ashrrev_i32_e32 v5, 31, v4
	s_barrier
	v_cndmask_b32_e32 v1, 0, v1, vcc
	v_add_u32_e32 v6, s81, v1
	v_add_u32_e32 v1, 0x60, v120
	v_cmp_gt_i32_e32 vcc, s80, v1
	v_ashrrev_i32_e32 v7, 31, v6
	s_nop 0
	v_cndmask_b32_e32 v1, 0, v1, vcc
	v_add_u32_e32 v8, s81, v1
	v_ashrrev_i32_e32 v9, 31, v8
	v_lshl_add_u64 v[4:5], v[4:5], 2, s[2:3]
	v_lshl_add_u64 v[6:7], v[6:7], 2, s[2:3]
	v_lshl_add_u64 v[8:9], v[8:9], 2, s[2:3]
	global_load_dword v16, v[2:3], off
	global_load_dword v18, v[4:5], off
	global_load_dword v20, v[6:7], off
	global_load_dword v22, v[8:9], off
	v_lshlrev_b32_e32 v24, 7, v0
	s_add_i32 s0, s79, 1
	s_lshl_b32 s14, s37, 22
	v_add_u32_e32 v2, 0x5000, v125
	s_ashr_i32 s37, s0, 1
	v_lshl_add_u64 v[0:1], v[98:99], 0, s[14:15]
	v_ashrrev_i32_e32 v25, 31, v24
	v_add_u32_e32 v3, 0x6000, v125
	v_readfirstlane_b32 s83, v2
	v_lshl_add_u64 v[0:1], v[24:25], 1, v[0:1]
	s_add_u32 s0, s8, s81
	v_add_u32_e32 v4, 0x7000, v125
	v_add_u32_e32 v5, 0x8000, v125
	v_readfirstlane_b32 s84, v3
	v_lshlrev_b64 v[2:3], 2, v[24:25]
	s_addc_u32 s1, s9, 0
	v_lshl_add_u64 v[0:1], v[0:1], 0, v[96:97]
	s_mov_b32 m0, s83
	s_mov_b32 s7, s15
	v_readfirstlane_b32 s85, v4
	v_readfirstlane_b32 s86, v5
	v_lshl_add_u64 v[2:3], s[0:1], 0, v[2:3]
	global_load_lds_dwordx4 v[0:1], off sc1
	v_lshl_add_u64 v[4:5], v[0:1], 0, s[16:17]
	s_mov_b32 m0, s84
	v_lshl_add_u64 v[6:7], v[0:1], 0, s[18:19]
	v_lshl_add_u64 v[26:27], v[0:1], 0, s[20:21]
	v_lshl_add_u64 v[0:1], v[2:3], 0, s[6:7]
	global_load_lds_dwordx4 v[4:5], off sc1
	s_mov_b32 m0, s85
	v_readfirstlane_b32 s82, v125
	v_readfirstlane_b32 s0, v0
	v_readfirstlane_b32 s1, v1
	global_load_lds_dwordx4 v[6:7], off sc1
	s_mov_b32 m0, s86
	s_nop 2
	global_load_dwordx4 v[12:15], v153, s[0:1]
	global_load_dwordx4 v[8:11], v153, s[0:1] offset:64
	global_load_dwordx4 v[4:7], v153, s[0:1] offset:128
	global_load_dwordx4 v[0:3], v153, s[0:1] offset:192
	v_lshlrev_b64 v[110:111], 1, v[24:25]
	global_load_lds_dwordx4 v[26:27], off sc1
	s_mov_b32 m0, s82
	s_waitcnt vmcnt(0)
	s_cmp_eq_u32 s100, 0
	s_cbranch_scc1 .Lpf_tile
	v_cvt_pk_f16_f32 v218, v218, v219
	v_cvt_pk_f16_f32 v219, v220, v221
	v_cvt_pk_f16_f32 v220, v222, v223
	v_cvt_pk_f16_f32 v221, v224, v225
	global_store_dwordx2 v217, v[218:219], s[94:95]
	global_store_dwordx2 v217, v[220:221], s[94:95] offset:512
	s_add_u32 s94, s94, 0x200000
	s_addc_u32 s95, s95, 0
	v_cvt_pk_f16_f32 v226, v226, v227
	v_cvt_pk_f16_f32 v227, v228, v229
	v_cvt_pk_f16_f32 v228, v230, v231
	v_cvt_pk_f16_f32 v229, v232, v233
	global_store_dwordx2 v217, v[226:227], s[94:95]
	global_store_dwordx2 v217, v[228:229], s[94:95] offset:512
	s_add_u32 s94, s94, 0x200000
	s_addc_u32 s95, s95, 0
	v_cvt_pk_f16_f32 v234, v234, v235
	v_cvt_pk_f16_f32 v235, v236, v237
	v_cvt_pk_f16_f32 v236, v238, v239
	v_cvt_pk_f16_f32 v237, v240, v241
	global_store_dwordx2 v217, v[234:235], s[94:95]
	global_store_dwordx2 v217, v[236:237], s[94:95] offset:512
	s_add_u32 s94, s94, 0x200000
	s_addc_u32 s95, s95, 0
	v_cvt_pk_f16_f32 v242, v242, v243
	v_cvt_pk_f16_f32 v243, v244, v245
	v_cvt_pk_f16_f32 v244, v246, v247
	v_cvt_pk_f16_f32 v245, v248, v249
	global_store_dwordx2 v217, v[242:243], s[94:95]
	global_store_dwordx2 v217, v[244:245], s[94:95] offset:512
	s_add_u32 s94, s94, 0x200000
	s_addc_u32 s95, s95, 0
	s_mov_b32 s100, 0
.Lpf_tile:
	v_ashrrev_i32_e32 v17, 31, v16
	v_lshlrev_b64 v[16:17], 11, v[16:17]
	v_lshl_add_u64 v[26:27], v[104:105], 0, v[16:17]
	v_ashrrev_i32_e32 v19, 31, v18
	global_load_lds_dwordx4 v[26:27], off sc1
	v_add_u32_e32 v26, 0x1000, v125
	v_ashrrev_i32_e32 v21, 31, v20
	v_lshlrev_b64 v[18:19], 11, v[18:19]
	v_readfirstlane_b32 s0, v26
	v_add_u32_e32 v26, 0x2000, v125
	v_ashrrev_i32_e32 v23, 31, v22
	v_lshlrev_b64 v[20:21], 11, v[20:21]
	v_lshl_add_u64 v[28:29], v[104:105], 0, v[18:19]
	s_mov_b32 m0, s0
	v_readfirstlane_b32 s0, v26
	v_add_u32_e32 v26, 0x3000, v125
	v_lshlrev_b64 v[22:23], 11, v[22:23]
	v_lshl_add_u64 v[30:31], v[104:105], 0, v[20:21]
	global_load_lds_dwordx4 v[28:29], off sc1
	s_mov_b32 m0, s0
	v_readfirstlane_b32 s0, v26
	v_lshl_add_u64 v[32:33], v[104:105], 0, v[22:23]
	global_load_lds_dwordx4 v[30:31], off sc1
	s_mov_b32 m0, s0
	s_and_b64 s[0:1], s[12:13], exec
	global_load_lds_dwordx4 v[32:33], off sc1
	s_cselect_b32 s7, 0, s37
	v_bitop3_b32 v27, s7, v152, 1 bitop3:0x6c
	v_lshl_or_b32 v26, s7, 11, v126
	v_lshlrev_b32_e32 v159, 4, v27
	s_cmp_lt_i32 s79, 9
	s_mov_b64 s[0:1], -1
	v_add_u32_e32 v156, 0, v26
	v_lshl_add_u64 v[112:113], v[106:107], 0, v[16:17]
	v_lshl_add_u64 v[114:115], v[106:107], 0, v[18:19]
	v_lshl_add_u64 v[116:117], v[106:107], 0, v[20:21]
	v_lshl_add_u64 v[118:119], v[106:107], 0, v[22:23]
	v_xor_b32_e32 v160, 16, v159
	v_xor_b32_e32 v158, 64, v159
	v_xor_b32_e32 v157, 0x50, v159
	s_cbranch_scc0 .LBB2_43
	v_lshl_add_u64 v[16:17], s[14:15], 0, v[110:111]
	v_lshl_add_u64 v[80:81], v[108:109], 0, v[16:17]
	v_mov_b32_e32 v16, 0
	s_mov_b32 s82, 1
	s_mov_b64 s[0:1], 0
	v_mov_b32_e32 v17, v16
	v_mov_b32_e32 v18, v16
	v_mov_b32_e32 v19, v16
	v_mov_b32_e32 v20, v16
	v_mov_b32_e32 v21, v16
	v_mov_b32_e32 v22, v16
	v_mov_b32_e32 v23, v16
	v_mov_b32_e32 v24, v16
	v_mov_b32_e32 v25, v16
	v_mov_b32_e32 v26, v16
	v_mov_b32_e32 v27, v16
	v_mov_b32_e32 v28, v16
	v_mov_b32_e32 v29, v16
	v_mov_b32_e32 v30, v16
	v_mov_b32_e32 v31, v16
	v_mov_b32_e32 v32, v16
	v_mov_b32_e32 v33, v16
	v_mov_b32_e32 v34, v16
	v_mov_b32_e32 v35, v16
	v_mov_b32_e32 v36, v16
	v_mov_b32_e32 v37, v16
	v_mov_b32_e32 v38, v16
	v_mov_b32_e32 v39, v16
	v_mov_b32_e32 v40, v16
	v_mov_b32_e32 v41, v16
	v_mov_b32_e32 v42, v16
	v_mov_b32_e32 v43, v16
	v_mov_b32_e32 v44, v16
	v_mov_b32_e32 v45, v16
	v_mov_b32_e32 v46, v16
	v_mov_b32_e32 v47, v16
	v_mov_b32_e32 v48, v16
	v_mov_b32_e32 v49, v16
	v_mov_b32_e32 v50, v16
	v_mov_b32_e32 v51, v16
	v_mov_b32_e32 v52, v16
	v_mov_b32_e32 v53, v16
	v_mov_b32_e32 v54, v16
	v_mov_b32_e32 v55, v16
	v_mov_b32_e32 v56, v16
	v_mov_b32_e32 v57, v16
	v_mov_b32_e32 v58, v16
	v_mov_b32_e32 v59, v16
	v_mov_b32_e32 v60, v16
	v_mov_b32_e32 v61, v16
	v_mov_b32_e32 v62, v16
	v_mov_b32_e32 v63, v16
	v_mov_b32_e32 v64, v16
	v_mov_b32_e32 v65, v16
	v_mov_b32_e32 v66, v16
	v_mov_b32_e32 v67, v16
	v_mov_b32_e32 v68, v16
	v_mov_b32_e32 v69, v16
	v_mov_b32_e32 v70, v16
	v_mov_b32_e32 v71, v16
	v_mov_b32_e32 v72, v16
	v_mov_b32_e32 v73, v16
	v_mov_b32_e32 v74, v16
	v_mov_b32_e32 v75, v16
	v_mov_b32_e32 v76, v16
	v_mov_b32_e32 v77, v16
	v_mov_b32_e32 v78, v16
	v_mov_b32_e32 v79, v16

.LBB2_78:
	s_mov_b64 exec, -1
	s_cmp_eq_u32 s100, 0
	s_cbranch_scc1 .Lpf_tail
	s_waitcnt vmcnt(0)
	v_cvt_pk_f16_f32 v218, v218, v219
	v_cvt_pk_f16_f32 v219, v220, v221
	v_cvt_pk_f16_f32 v220, v222, v223
	v_cvt_pk_f16_f32 v221, v224, v225
	global_store_dwordx2 v217, v[218:219], s[94:95]
	global_store_dwordx2 v217, v[220:221], s[94:95] offset:512
	s_add_u32 s94, s94, 0x200000
	s_addc_u32 s95, s95, 0
	v_cvt_pk_f16_f32 v226, v226, v227
	v_cvt_pk_f16_f32 v227, v228, v229
	v_cvt_pk_f16_f32 v228, v230, v231
	v_cvt_pk_f16_f32 v229, v232, v233
	global_store_dwordx2 v217, v[226:227], s[94:95]
	global_store_dwordx2 v217, v[228:229], s[94:95] offset:512
	s_add_u32 s94, s94, 0x200000
	s_addc_u32 s95, s95, 0
	v_cvt_pk_f16_f32 v234, v234, v235
	v_cvt_pk_f16_f32 v235, v236, v237
	v_cvt_pk_f16_f32 v236, v238, v239
	v_cvt_pk_f16_f32 v237, v240, v241
	global_store_dwordx2 v217, v[234:235], s[94:95]
	global_store_dwordx2 v217, v[236:237], s[94:95] offset:512
	s_add_u32 s94, s94, 0x200000
	s_addc_u32 s95, s95, 0
	v_cvt_pk_f16_f32 v242, v242, v243
	v_cvt_pk_f16_f32 v243, v244, v245
	v_cvt_pk_f16_f32 v244, v246, v247
	v_cvt_pk_f16_f32 v245, v248, v249
	global_store_dwordx2 v217, v[242:243], s[94:95]
	global_store_dwordx2 v217, v[244:245], s[94:95] offset:512
	s_add_u32 s94, s94, 0x200000
	s_addc_u32 s95, s95, 0
	s_mov_b32 s100, 0
.Lpf_tail:
.Lw2k_tail:
	s_cmp_eq_u32 s96, 0
	s_cbranch_scc1 .Lw2k_end
	s_mov_b32 s26, 0
	s_cmp_eq_u32 s96, 0
	s_cbranch_scc1 .Lw2k_tissued
	s_mov_b64 s[30:31], s[92:93]
	s_mov_b64 s[32:33], s[94:95]
	global_load_dwordx4 v[8:11], v216, s[30:31] nt
	global_load_dwordx4 v[12:15], v216, s[30:31] offset:1024 nt
	s_add_u32 s92, s92, 0x400000
	s_addc_u32 s93, s93, 0
	s_add_u32 s94, s94, 0x200000
	s_addc_u32 s95, s95, 0
	s_sub_u32 s96, s96, 1
	s_add_i32 s26, s26, 1
	s_cmp_eq_u32 s96, 0
	s_cbranch_scc1 .Lw2k_tissued
	s_mov_b64 s[34:35], s[92:93]
	s_mov_b64 s[36:37], s[94:95]
	global_load_dwordx4 v[16:19], v216, s[34:35] nt
	global_load_dwordx4 v[20:23], v216, s[34:35] offset:1024 nt
	s_add_u32 s92, s92, 0x400000
	s_addc_u32 s93, s93, 0
	s_add_u32 s94, s94, 0x200000
	s_addc_u32 s95, s95, 0
	s_sub_u32 s96, s96, 1
	s_add_i32 s26, s26, 1
	s_cmp_eq_u32 s96, 0
	s_cbranch_scc1 .Lw2k_tissued
	s_mov_b64 s[38:39], s[92:93]
	s_mov_b64 s[40:41], s[94:95]
	global_load_dwordx4 v[24:27], v216, s[38:39] nt
	global_load_dwordx4 v[28:31], v216, s[38:39] offset:1024 nt
	s_add_u32 s92, s92, 0x400000
	s_addc_u32 s93, s93, 0
	s_add_u32 s94, s94, 0x200000
	s_addc_u32 s95, s95, 0
	s_sub_u32 s96, s96, 1
	s_add_i32 s26, s26, 1
	s_cmp_eq_u32 s96, 0
	s_cbranch_scc1 .Lw2k_tissued
	s_mov_b64 s[42:43], s[92:93]
	s_mov_b64 s[44:45], s[94:95]
	global_load_dwordx4 v[32:35], v216, s[42:43] nt
	global_load_dwordx4 v[36:39], v216, s[42:43] offset:1024 nt
	s_add_u32 s92, s92, 0x400000
	s_addc_u32 s93, s93, 0
	s_add_u32 s94, s94, 0x200000
	s_addc_u32 s95, s95, 0
	s_sub_u32 s96, s96, 1
	s_add_i32 s26, s26, 1
	s_cmp_eq_u32 s96, 0
	s_cbranch_scc1 .Lw2k_tissued
	s_mov_b64 s[46:47], s[92:93]
	s_mov_b64 s[48:49], s[94:95]
	global_load_dwordx4 v[40:43], v216, s[46:47] nt
	global_load_dwordx4 v[44:47], v216, s[46:47] offset:1024 nt
	s_add_u32 s92, s92, 0x400000
	s_addc_u32 s93, s93, 0
	s_add_u32 s94, s94, 0x200000
	s_addc_u32 s95, s95, 0
	s_sub_u32 s96, s96, 1
	s_add_i32 s26, s26, 1
	s_cmp_eq_u32 s96, 0
	s_cbranch_scc1 .Lw2k_tissued
	s_mov_b64 s[50:51], s[92:93]
	s_mov_b64 s[52:53], s[94:95]
	global_load_dwordx4 v[48:51], v216, s[50:51] nt
	global_load_dwordx4 v[52:55], v216, s[50:51] offset:1024 nt
	s_add_u32 s92, s92, 0x400000
	s_addc_u32 s93, s93, 0
	s_add_u32 s94, s94, 0x200000
	s_addc_u32 s95, s95, 0
	s_sub_u32 s96, s96, 1
	s_add_i32 s26, s26, 1
	s_cmp_eq_u32 s96, 0
	s_cbranch_scc1 .Lw2k_tissued
	s_mov_b64 s[54:55], s[92:93]
	s_mov_b64 s[56:57], s[94:95]
	global_load_dwordx4 v[56:59], v216, s[54:55] nt
	global_load_dwordx4 v[60:63], v216, s[54:55] offset:1024 nt
	s_add_u32 s92, s92, 0x400000
	s_addc_u32 s93, s93, 0
	s_add_u32 s94, s94, 0x200000
	s_addc_u32 s95, s95, 0
	s_sub_u32 s96, s96, 1
	s_add_i32 s26, s26, 1
	s_cmp_eq_u32 s96, 0
	s_cbranch_scc1 .Lw2k_tissued
	s_mov_b64 s[58:59], s[92:93]
	s_mov_b64 s[60:61], s[94:95]
	global_load_dwordx4 v[64:67], v216, s[58:59] nt
	global_load_dwordx4 v[68:71], v216, s[58:59] offset:1024 nt
	s_add_u32 s92, s92, 0x400000
	s_addc_u32 s93, s93, 0
	s_add_u32 s94, s94, 0x200000
	s_addc_u32 s95, s95, 0
	s_sub_u32 s96, s96, 1
	s_add_i32 s26, s26, 1

	.amdhsa_kernel _Z8moe_gemmILi1024ELi2048ELb1EEvPKDF16_S1_PKfPDF16_PfPKiS7_
		.amdhsa_group_segment_fixed_size 0
		.amdhsa_private_segment_fixed_size 0
		.amdhsa_kernarg_size 312
		.amdhsa_user_sgpr_count 2
		.amdhsa_user_sgpr_dispatch_ptr 0
		.amdhsa_user_sgpr_queue_ptr 0
		.amdhsa_user_sgpr_kernarg_segment_ptr 1
		.amdhsa_user_sgpr_dispatch_id 0
		.amdhsa_user_sgpr_kernarg_preload_length 0
		.amdhsa_user_sgpr_kernarg_preload_offset 0
		.amdhsa_user_sgpr_private_segment_size 0
		.amdhsa_uses_dynamic_stack 0
		.amdhsa_enable_private_segment 0
		.amdhsa_system_sgpr_workgroup_id_x 1
		.amdhsa_system_sgpr_workgroup_id_y 0
		.amdhsa_system_sgpr_workgroup_id_z 0
		.amdhsa_system_sgpr_workgroup_info 0
		.amdhsa_system_vgpr_workitem_id 0
		.amdhsa_next_free_vgpr 250
		.amdhsa_next_free_sgpr 102
		.amdhsa_accum_offset 252
		.amdhsa_reserve_vcc 1
		.amdhsa_float_round_mode_32 0
		.amdhsa_float_round_mode_16_64 0
		.amdhsa_float_denorm_mode_32 3
		.amdhsa_float_denorm_mode_16_64 3
		.amdhsa_dx10_clamp 1
		.amdhsa_ieee_mode 1
		.amdhsa_fp16_overflow 0
		.amdhsa_tg_split 0
		.amdhsa_exception_fp_ieee_invalid_op 0
		.amdhsa_exception_fp_denorm_src 0
		.amdhsa_exception_fp_ieee_div_zero 0
		.amdhsa_exception_fp_ieee_overflow 0
		.amdhsa_exception_fp_ieee_underflow 0
		.amdhsa_exception_fp_ieee_inexact 0
		.amdhsa_exception_int_div_zero 0
	.end_amdhsa_kernel

amdhsa.kernels:
  - .agpr_count:     0
    .args:
      - .actual_access:  read_only
        .address_space:  global
        .offset:         0
        .size:           8
        .value_kind:     global_buffer
      - .address_space:  global
        .offset:         8
        .size:           8
        .value_kind:     global_buffer
      - .actual_access:  read_only
        .address_space:  global
        .offset:         16
        .size:           8
        .value_kind:     global_buffer
      - .address_space:  global
        .offset:         24
        .size:           8
        .value_kind:     global_buffer
      - .offset:         32
        .size:           4
        .value_kind:     by_value
      - .actual_access:  write_only
        .address_space:  global
        .offset:         40
        .size:           8
        .value_kind:     global_buffer
      - .offset:         48
        .size:           4
        .value_kind:     hidden_block_count_x
      - .offset:         52
        .size:           4
        .value_kind:     hidden_block_count_y
      - .offset:         56
        .size:           4
        .value_kind:     hidden_block_count_z
      - .offset:         60
        .size:           2
        .value_kind:     hidden_group_size_x
      - .offset:         62
        .size:           2
        .value_kind:     hidden_group_size_y
      - .offset:         64
        .size:           2
        .value_kind:     hidden_group_size_z
      - .offset:         66
        .size:           2
        .value_kind:     hidden_remainder_x
      - .offset:         68
        .size:           2
        .value_kind:     hidden_remainder_y
      - .offset:         70
        .size:           2
        .value_kind:     hidden_remainder_z
      - .offset:         88
        .size:           8
        .value_kind:     hidden_global_offset_x
      - .offset:         96
        .size:           8
        .value_kind:     hidden_global_offset_y
      - .offset:         104
        .size:           8
        .value_kind:     hidden_global_offset_z
      - .offset:         112
        .size:           2
        .value_kind:     hidden_grid_dims
    .group_segment_fixed_size: 0
    .kernarg_segment_align: 8
    .kernarg_segment_size: 304
    .language:       OpenCL C
    .language_version:
      - 2
      - 0
    .max_flat_workgroup_size: 256
    .name:           _Z5cvt_wPKfPDF16_S0_S1_iPi
    .private_segment_fixed_size: 0
    .sgpr_count:     30
    .sgpr_spill_count: 0
    .symbol:         _Z5cvt_wPKfPDF16_S0_S1_iPi.kd
    .uniform_work_group_size: 1
    .uses_dynamic_stack: false
    .vgpr_count:     40
    .vgpr_spill_count: 0
    .wavefront_size: 64
  - .agpr_count:     0
    .args:
      - .actual_access:  read_only
        .address_space:  global
        .offset:         0
        .size:           8
        .value_kind:     global_buffer
      - .actual_access:  read_only
        .address_space:  global
        .offset:         8
        .size:           8
        .value_kind:     global_buffer
      - .actual_access:  read_only
        .address_space:  global
        .offset:         16
        .size:           8
        .value_kind:     global_buffer
      - .actual_access:  write_only
        .address_space:  global
        .offset:         24
        .size:           8
        .value_kind:     global_buffer
      - .address_space:  global
        .offset:         32
        .size:           8
        .value_kind:     global_buffer
      - .actual_access:  write_only
        .address_space:  global
        .offset:         40
        .size:           8
        .value_kind:     global_buffer
      - .actual_access:  write_only
        .address_space:  global
        .offset:         48
        .size:           8
        .value_kind:     global_buffer
      - .actual_access:  read_only
        .address_space:  global
        .offset:         56
        .size:           8
        .value_kind:     global_buffer
      - .address_space:  global
        .offset:         64
        .size:           8
        .value_kind:     global_buffer
      - .offset:         72
        .size:           4
        .value_kind:     by_value
      - .offset:         80
        .size:           4
        .value_kind:     hidden_block_count_x
      - .offset:         84
        .size:           4
        .value_kind:     hidden_block_count_y
      - .offset:         88
        .size:           4
        .value_kind:     hidden_block_count_z
      - .offset:         92
        .size:           2
        .value_kind:     hidden_group_size_x
      - .offset:         94
        .size:           2
        .value_kind:     hidden_group_size_y
      - .offset:         96
        .size:           2
        .value_kind:     hidden_group_size_z
      - .offset:         98
        .size:           2
        .value_kind:     hidden_remainder_x
      - .offset:         100
        .size:           2
        .value_kind:     hidden_remainder_y
      - .offset:         102
        .size:           2
        .value_kind:     hidden_remainder_z
      - .offset:         120
        .size:           8
        .value_kind:     hidden_global_offset_x
      - .offset:         128
        .size:           8
        .value_kind:     hidden_global_offset_y
      - .offset:         136
        .size:           8
        .value_kind:     hidden_global_offset_z
      - .offset:         144
        .size:           2
        .value_kind:     hidden_grid_dims
    .group_segment_fixed_size: 32928
    .kernarg_segment_align: 8
    .kernarg_segment_size: 336
    .language:       OpenCL C
    .language_version:
      - 2
      - 0
    .max_flat_workgroup_size: 512
    .name:           _Z11gate_kernelPKfS0_S0_PDF16_PiS2_PfS0_S1_i
    .private_segment_fixed_size: 0
    .sgpr_count:     66
    .sgpr_spill_count: 0
    .symbol:         _Z11gate_kernelPKfS0_S0_PDF16_PiS2_PfS0_S1_i.kd
    .uniform_work_group_size: 1
    .uses_dynamic_stack: false
    .vgpr_count:     115
    .vgpr_spill_count: 0
    .wavefront_size: 64
  - .agpr_count:     0
    .args:
      - .address_space:  global
        .offset:         0
        .size:           8
        .value_kind:     global_buffer
      - .address_space:  global
        .offset:         8
        .size:           8
        .value_kind:     global_buffer
      - .actual_access:  read_only
        .address_space:  global
        .offset:         16
        .size:           8
        .value_kind:     global_buffer
      - .address_space:  global
        .offset:         24
        .size:           8
        .value_kind:     global_buffer
      - .actual_access:  read_only
        .address_space:  global
        .offset:         32
        .size:           8
        .value_kind:     global_buffer
      - .actual_access:  read_only
        .address_space:  global
        .offset:         40
        .size:           8
        .value_kind:     global_buffer
      - .actual_access:  read_only
        .address_space:  global
        .offset:         48
        .size:           8
        .value_kind:     global_buffer
      - .offset:         56
        .size:           4
        .value_kind:     hidden_block_count_x
      - .offset:         60
        .size:           4
        .value_kind:     hidden_block_count_y
      - .offset:         64
        .size:           4
        .value_kind:     hidden_block_count_z
      - .offset:         68
        .size:           2
        .value_kind:     hidden_group_size_x
      - .offset:         70
        .size:           2
        .value_kind:     hidden_group_size_y
      - .offset:         72
        .size:           2
        .value_kind:     hidden_group_size_z
      - .offset:         74
        .size:           2
        .value_kind:     hidden_remainder_x
      - .offset:         76
        .size:           2
        .value_kind:     hidden_remainder_y
      - .offset:         78
        .size:           2
        .value_kind:     hidden_remainder_z
      - .offset:         96
        .size:           8
        .value_kind:     hidden_global_offset_x
      - .offset:         104
        .size:           8
        .value_kind:     hidden_global_offset_y
      - .offset:         112
        .size:           8
        .value_kind:     hidden_global_offset_z
      - .offset:         120
        .size:           2
        .value_kind:     hidden_grid_dims
      - .offset:         176
        .size:           4
        .value_kind:     hidden_dynamic_lds_size
    .group_segment_fixed_size: 0
    .kernarg_segment_align: 8
    .kernarg_segment_size: 312
    .language:       OpenCL C
    .language_version:
      - 2
      - 0
    .max_flat_workgroup_size: 256
    .name:           _Z8moe_gemmILi1024ELi2048ELb1EEvPKDF16_S1_PKfPDF16_PfPKiS7_
    .private_segment_fixed_size: 0
    .sgpr_count:     108
    .sgpr_spill_count: 0
    .symbol:         _Z8moe_gemmILi1024ELi2048ELb1EEvPKDF16_S1_PKfPDF16_PfPKiS7_.kd
    .uniform_work_group_size: 1
    .uses_dynamic_stack: false
    .vgpr_count:     250
    .vgpr_spill_count: 0
    .wavefront_size: 64
  - .agpr_count:     256
    .args:
      - .address_space:  global
        .offset:         0
        .size:           8
        .value_kind:     global_buffer
      - .address_space:  global
        .offset:         8
        .size:           8
        .value_kind:     global_buffer
      - .actual_access:  read_only
        .address_space:  global
        .offset:         16
        .size:           8
        .value_kind:     global_buffer
      - .actual_access:  read_only
        .address_space:  global
        .offset:         24
        .size:           8
        .value_kind:     global_buffer
      - .address_space:  global
        .offset:         32
        .size:           8
        .value_kind:     global_buffer
      - .actual_access:  read_only
        .address_space:  global
        .offset:         40
        .size:           8
        .value_kind:     global_buffer
      - .actual_access:  read_only
        .address_space:  global
        .offset:         48
        .size:           8
        .value_kind:     global_buffer
      - .offset:         56
        .size:           4
        .value_kind:     hidden_block_count_x
      - .offset:         60
        .size:           4
        .value_kind:     hidden_block_count_y
      - .offset:         64
        .size:           4
        .value_kind:     hidden_block_count_z
      - .offset:         68
        .size:           2
        .value_kind:     hidden_group_size_x
      - .offset:         70
        .size:           2
        .value_kind:     hidden_group_size_y
      - .offset:         72
        .size:           2
        .value_kind:     hidden_group_size_z
      - .offset:         74
        .size:           2
        .value_kind:     hidden_remainder_x
      - .offset:         76
        .size:           2
        .value_kind:     hidden_remainder_y
      - .offset:         78
        .size:           2
        .value_kind:     hidden_remainder_z
      - .offset:         96
        .size:           8
        .value_kind:     hidden_global_offset_x
      - .offset:         104
        .size:           8
        .value_kind:     hidden_global_offset_y
      - .offset:         112
        .size:           8
        .value_kind:     hidden_global_offset_z
      - .offset:         120
        .size:           2
        .value_kind:     hidden_grid_dims
      - .offset:         176
        .size:           4
        .value_kind:     hidden_dynamic_lds_size
    .group_segment_fixed_size: 86016
    .kernarg_segment_align: 8
    .kernarg_segment_size: 312
    .language:       OpenCL C
    .language_version:
      - 2
      - 0
    .max_flat_workgroup_size: 256
    .name:           _Z8moe_gemmILi2048ELi1024ELb0EEvPKDF16_S1_PKfPDF16_PfPKiS7_
    .private_segment_fixed_size: 0
    .sgpr_count:     96
    .sgpr_spill_count: 0
    .symbol:         _Z8moe_gemmILi2048ELi1024ELb0EEvPKDF16_S1_PKfPDF16_PfPKiS7_.kd
    .uniform_work_group_size: 1
    .uses_dynamic_stack: false
    .vgpr_count:     512
    .vgpr_spill_count: 0
    .wavefront_size: 64
